# MLA units assigned statically (unit = workgroup id: 256 units, 256 workgroups): no device-atomic claim at the start of the attention phase, and each XCD works on one (batch, head) so its K/V stream st
# speedup vs baseline: 1.0017x; 1.0017x over previous
; __device__ __forceinline__ void claim_fire(unsigned* ctr, int tid, int* pend) { if (tid == 0) *pend = (int)__hip_atomic_fetch_add(ctr, 1u, __ATOMIC_RELAXED, __HIP_MEMORY_SCOPE_AGENT); }
;     ...
;     const int* pos = (const int*)a->in[1];
;     unsigned* q0ctr = F.ctl + CW_QUEUE + ((l + qlo) * 8 + 0 + qs) * 64; unsigned* q1ctr = F.ctl + CW_QUEUE + ((l + qlo) * 8 + 1 + qs) * 64;
;     const bf16_t* QA = (const bf16_t*)(F.ws + WS_QA); const bf16_t* KAp = (const bf16_t*)(F.ws + WS_KA); const bf16_t* VAp = (const bf16_t*)(F.ws + WS_VA);
;     bf16_t* O = (bf16_t*)(F.ws + WS_O);
;     int pend = 0, lastm = 1 << 20;
;     at::claim_fire(q0ctr, F.tid, &pend);
; __global__ void __launch_bounds__(NTHR, 2) mk_fwd(Args args) {
;     ...
;         if (RUN(PH_ATTN1)) phase_attn1(lds, wv, l);
.LBB0_853:
	v_readlane_b32 s40, v254, 62
	s_cmp_ge_i32 s1, s40
	s_cselect_b64 s[2:3], -1, 0
	v_readlane_b32 s42, v255, 0
	v_readlane_b32 s43, v255, 1
	v_writelane_b32 v255, s2, 5
	v_readlane_b32 s41, v254, 63
	s_nop 0
	v_writelane_b32 v255, s3, 6
	s_and_b64 s[2:3], s[2:3], s[10:11]
	s_andn2_b64 vcc, exec, s[2:3]
	s_cbranch_vccnz .LBB0_1112
	v_readlane_b32 s24, v253, 0
	v_readlane_b32 s25, v253, 1
	s_mov_b64 s[2:3], s[24:25]
	s_load_dwordx2 s[50:51], s[2:3], 0xf0
	s_lshl_b32 s2, s72, 9
	s_mov_b32 s1, -1
	s_mov_b64 s[46:47], s[24:25]
	s_ashr_i32 s3, s2, 31
	s_load_dwordx2 s[6:7], s[46:47], 0x8
	s_waitcnt lgkmcnt(0)
	v_mbcnt_lo_u32_b32 v0, s1, 0
	s_lshl_b64 s[2:3], s[2:3], 2
	v_mbcnt_hi_u32_b32 v0, s1, v0
	s_waitcnt lgkmcnt(0)
	s_add_u32 s1, s50, s2
	s_addc_u32 s2, s51, s3
	s_add_u32 s52, s1, 0x3000
	v_readlane_b32 s1, v253, 8
	s_waitcnt vmcnt(0)
	v_mov_b32_e32 v164, 0
	s_addc_u32 s53, s2, 0
	v_cmp_eq_u32_e64 s[38:39], s1, v0
	s_and_saveexec_b64 s[10:11], s[38:39]
	s_cbranch_execz .LBB0_858
	s_mov_b64 s[16:17], exec
	v_mbcnt_lo_u32_b32 v0, s16, 0
	v_mbcnt_hi_u32_b32 v0, s17, v0
	v_cmp_eq_u32_e32 vcc, 0, v0
	s_and_saveexec_b64 s[14:15], vcc
	s_cbranch_execz .LBB0_857
	s_bcnt1_i32_b64 s1, s[16:17]
	v_mov_b32_e32 v1, s1
	v_mov_b32_e32 v1, s92
	s_nop 0

;     ...
;     if (nctr != nullptr && tid == 0) *pend = (int)__hip_atomic_fetch_add(nctr, 1u, __ATOMIC_RELAXED, __HIP_MEMORY_SCOPE_AGENT);
;     ...
;         const int idx = at::claim_take(lds, F.tid, &pend); if (idx >= 256) break;
.LBB0_888:
	v_cmp_eq_u32_e32 vcc, 0, v29
	s_and_saveexec_b64 s[14:15], vcc
	s_cbranch_execz .LBB0_892
	s_mov_b64 s[34:35], exec
	v_mbcnt_lo_u32_b32 v16, s34, 0
	v_mbcnt_hi_u32_b32 v16, s35, v16
	v_cmp_eq_u32_e32 vcc, 0, v16
	s_and_saveexec_b64 s[16:17], vcc
	s_cbranch_execz .LBB0_891
	s_bcnt1_i32_b64 s34, s[34:35]
	v_mov_b32_e32 v17, s34
	v_mov_b32_e32 v192, 0x100
